# v33 + down-GEMM epilogue: store base address computed once, other three store groups = base + const (20 fewer 64-bit VALU ops per wave per unit)
# baseline (speedup 1.0000x reference)
.LBB0_52:
	s_nop 15
	s_nop 15
	v_lshl_add_u32 v22, s62, 8, v186
	v_ashrrev_i32_e32 v23, 31, v22
	s_ashr_i32 s27, s26, 31
	s_add_u32 s100, s40, s26
	s_addc_u32 s101, s41, s27
	s_add_u32 s100, s100, s94
	s_addc_u32 s101, s101, s95
	v_lshlrev_b64 v[250:251], 10, v[22:23]
	v_lshl_add_u64 v[250:251], v[250:251], 0, s[100:101]
	v_lshl_add_u64 v[250:251], v[250:251], 0, v[168:169]
	s_andn2_b64 vcc, exec, s[54:55]
	s_waitcnt vmcnt(0)
	v_pk_fma_f32 v[28:29], v[154:155], s[24:25], v[10:11] op_sel_hi:[1,0,1]
	v_pk_fma_f32 v[24:25], v[158:159], s[24:25], v[14:15] op_sel_hi:[1,0,1]
	v_cvt_pk_fp8_f32 v19, v28, v29
	v_cvt_pk_fp8_f32 v18, v24, v25
	v_pk_fma_f32 v[20:21], v[160:161], s[24:25], v[16:17] op_sel_hi:[1,0,1]
	v_pk_fma_f32 v[26:27], v[156:157], s[24:25], v[12:13] op_sel_hi:[1,0,1]
	v_pk_fma_f32 v[30:31], v[146:147], s[24:25], v[10:11] op_sel_hi:[1,0,1]
	v_cvt_pk_fp8_f32 v18, v20, v21 op_sel:[0,0,1]
	v_cvt_pk_fp8_f32 v19, v26, v27 op_sel:[0,0,1]
	v_pk_fma_f32 v[26:27], v[150:151], s[24:25], v[14:15] op_sel_hi:[1,0,1]
	v_cvt_pk_fp8_f32 v20, v26, v27
	v_cvt_pk_fp8_f32 v21, v30, v31
	v_pk_fma_f32 v[24:25], v[152:153], s[24:25], v[16:17] op_sel_hi:[1,0,1]
	v_pk_fma_f32 v[28:29], v[148:149], s[24:25], v[12:13] op_sel_hi:[1,0,1]
	v_cvt_pk_fp8_f32 v20, v24, v25 op_sel:[0,0,1]
	v_cvt_pk_fp8_f32 v21, v28, v29 op_sel:[0,0,1]
	v_permlane16_swap_b32_e32 v18, v20
	v_permlane16_swap_b32_e32 v19, v21
	global_store_dwordx4 v[250:251], v[18:21], off
	v_pk_fma_f32 v[26:27], v[142:143], s[24:25], v[6:7] op_sel_hi:[1,0,1]
	v_pk_fma_f32 v[30:31], v[138:139], s[24:25], v[2:3] op_sel_hi:[1,0,1]
	v_cvt_pk_fp8_f32 v18, v26, v27
	v_cvt_pk_fp8_f32 v19, v30, v31
	v_pk_fma_f32 v[20:21], v[144:145], s[24:25], v[8:9] op_sel_hi:[1,0,1]
	v_pk_fma_f32 v[28:29], v[140:141], s[24:25], v[4:5] op_sel_hi:[1,0,1]
	v_cvt_pk_fp8_f32 v18, v20, v21 op_sel:[0,0,1]
	v_cvt_pk_fp8_f32 v19, v28, v29 op_sel:[0,0,1]
	v_pk_fma_f32 v[28:29], v[134:135], s[24:25], v[6:7] op_sel_hi:[1,0,1]
	v_pk_fma_f32 v[32:33], v[130:131], s[24:25], v[2:3] op_sel_hi:[1,0,1]
	v_cvt_pk_fp8_f32 v20, v28, v29
	v_cvt_pk_fp8_f32 v21, v32, v33
	v_pk_fma_f32 v[26:27], v[136:137], s[24:25], v[8:9] op_sel_hi:[1,0,1]
	v_pk_fma_f32 v[30:31], v[132:133], s[24:25], v[4:5] op_sel_hi:[1,0,1]
	v_cvt_pk_fp8_f32 v20, v26, v27 op_sel:[0,0,1]
	v_cvt_pk_fp8_f32 v21, v30, v31 op_sel:[0,0,1]
	v_pk_fma_f32 v[26:27], v[126:127], s[24:25], v[14:15] op_sel_hi:[1,0,1]
	v_pk_fma_f32 v[30:31], v[122:123], s[24:25], v[10:11] op_sel_hi:[1,0,1]
	v_permlane16_swap_b32_e32 v18, v20
	v_permlane16_swap_b32_e32 v19, v21
	global_store_dwordx4 v[250:251], v[18:21], off offset:128
	v_pk_fma_f32 v[32:33], v[114:115], s[24:25], v[10:11] op_sel_hi:[1,0,1]
	v_cvt_pk_fp8_f32 v18, v26, v27
	v_pk_fma_f32 v[20:21], v[128:129], s[24:25], v[16:17] op_sel_hi:[1,0,1]
	v_cvt_pk_fp8_f32 v19, v30, v31
	v_cvt_pk_fp8_f32 v18, v20, v21 op_sel:[0,0,1]
	v_pk_fma_f32 v[30:31], v[118:119], s[24:25], v[14:15] op_sel_hi:[1,0,1]
	v_cvt_pk_fp8_f32 v20, v30, v31
	v_cvt_pk_fp8_f32 v21, v32, v33
	v_pk_fma_f32 v[28:29], v[124:125], s[24:25], v[12:13] op_sel_hi:[1,0,1]
	v_cvt_pk_fp8_f32 v19, v28, v29 op_sel:[0,0,1]
	v_pk_fma_f32 v[28:29], v[120:121], s[24:25], v[16:17] op_sel_hi:[1,0,1]
	v_pk_fma_f32 v[26:27], v[116:117], s[24:25], v[12:13] op_sel_hi:[1,0,1]
	v_cvt_pk_fp8_f32 v20, v28, v29 op_sel:[0,0,1]
	v_cvt_pk_fp8_f32 v21, v26, v27 op_sel:[0,0,1]
	v_permlane16_swap_b32_e32 v18, v20
	v_permlane16_swap_b32_e32 v19, v21
	s_mov_b64 s[100:101], 0x8000
	v_lshl_add_u64 v[24:25], v[250:251], 0, s[100:101]
	global_store_dwordx4 v[24:25], v[18:21], off
	v_pk_fma_f32 v[26:27], v[110:111], s[24:25], v[6:7] op_sel_hi:[1,0,1]
	v_pk_fma_f32 v[30:31], v[106:107], s[24:25], v[2:3] op_sel_hi:[1,0,1]
	v_cvt_pk_fp8_f32 v18, v26, v27
	v_cvt_pk_fp8_f32 v19, v30, v31
	v_pk_fma_f32 v[20:21], v[112:113], s[24:25], v[8:9] op_sel_hi:[1,0,1]
	v_pk_fma_f32 v[28:29], v[108:109], s[24:25], v[4:5] op_sel_hi:[1,0,1]
	v_cvt_pk_fp8_f32 v18, v20, v21 op_sel:[0,0,1]
	v_cvt_pk_fp8_f32 v19, v28, v29 op_sel:[0,0,1]
	v_pk_fma_f32 v[28:29], v[102:103], s[24:25], v[6:7] op_sel_hi:[1,0,1]
	v_pk_fma_f32 v[32:33], v[98:99], s[24:25], v[2:3] op_sel_hi:[1,0,1]
	v_cvt_pk_fp8_f32 v20, v28, v29
	v_cvt_pk_fp8_f32 v21, v32, v33
	v_pk_fma_f32 v[26:27], v[104:105], s[24:25], v[8:9] op_sel_hi:[1,0,1]
	v_pk_fma_f32 v[30:31], v[100:101], s[24:25], v[4:5] op_sel_hi:[1,0,1]
	v_cvt_pk_fp8_f32 v20, v26, v27 op_sel:[0,0,1]
	v_cvt_pk_fp8_f32 v21, v30, v31 op_sel:[0,0,1]
	v_pk_fma_f32 v[26:27], v[94:95], s[24:25], v[14:15] op_sel_hi:[1,0,1]
	v_pk_fma_f32 v[30:31], v[90:91], s[24:25], v[10:11] op_sel_hi:[1,0,1]
	v_permlane16_swap_b32_e32 v18, v20
	v_permlane16_swap_b32_e32 v19, v21
	global_store_dwordx4 v[24:25], v[18:21], off offset:128
	v_pk_fma_f32 v[28:29], v[92:93], s[24:25], v[12:13] op_sel_hi:[1,0,1]
	v_pk_fma_f32 v[32:33], v[82:83], s[24:25], v[10:11] op_sel_hi:[1,0,1]
	v_cvt_pk_fp8_f32 v18, v26, v27
	v_cvt_pk_fp8_f32 v19, v30, v31
	v_pk_fma_f32 v[20:21], v[96:97], s[24:25], v[16:17] op_sel_hi:[1,0,1]
	v_cvt_pk_fp8_f32 v18, v20, v21 op_sel:[0,0,1]
	v_cvt_pk_fp8_f32 v19, v28, v29 op_sel:[0,0,1]
	v_pk_fma_f32 v[28:29], v[86:87], s[24:25], v[14:15] op_sel_hi:[1,0,1]
	v_cvt_pk_fp8_f32 v20, v28, v29
	v_cvt_pk_fp8_f32 v21, v32, v33
	v_pk_fma_f32 v[26:27], v[88:89], s[24:25], v[16:17] op_sel_hi:[1,0,1]
	v_pk_fma_f32 v[30:31], v[84:85], s[24:25], v[12:13] op_sel_hi:[1,0,1]
	v_cvt_pk_fp8_f32 v20, v26, v27 op_sel:[0,0,1]
	v_cvt_pk_fp8_f32 v21, v30, v31 op_sel:[0,0,1]
	v_permlane16_swap_b32_e32 v18, v20
	v_permlane16_swap_b32_e32 v19, v21
	s_mov_b64 s[100:101], 0x20000
	v_lshl_add_u64 v[24:25], v[250:251], 0, s[100:101]
	global_store_dwordx4 v[24:25], v[18:21], off
	v_pk_fma_f32 v[26:27], v[78:79], s[24:25], v[6:7] op_sel_hi:[1,0,1]
	v_pk_fma_f32 v[30:31], v[74:75], s[24:25], v[2:3] op_sel_hi:[1,0,1]
	v_cvt_pk_fp8_f32 v18, v26, v27
	v_cvt_pk_fp8_f32 v19, v30, v31
	v_pk_fma_f32 v[20:21], v[80:81], s[24:25], v[8:9] op_sel_hi:[1,0,1]
	v_pk_fma_f32 v[28:29], v[76:77], s[24:25], v[4:5] op_sel_hi:[1,0,1]
	v_cvt_pk_fp8_f32 v18, v20, v21 op_sel:[0,0,1]
	v_cvt_pk_fp8_f32 v19, v28, v29 op_sel:[0,0,1]
	v_pk_fma_f32 v[28:29], v[70:71], s[24:25], v[6:7] op_sel_hi:[1,0,1]
	v_pk_fma_f32 v[32:33], v[66:67], s[24:25], v[2:3] op_sel_hi:[1,0,1]
	v_cvt_pk_fp8_f32 v20, v28, v29
	v_cvt_pk_fp8_f32 v21, v32, v33
	v_pk_fma_f32 v[26:27], v[72:73], s[24:25], v[8:9] op_sel_hi:[1,0,1]
	v_pk_fma_f32 v[30:31], v[68:69], s[24:25], v[4:5] op_sel_hi:[1,0,1]
	v_cvt_pk_fp8_f32 v20, v26, v27 op_sel:[0,0,1]
	v_cvt_pk_fp8_f32 v21, v30, v31 op_sel:[0,0,1]
	v_permlane16_swap_b32_e32 v18, v20
	v_permlane16_swap_b32_e32 v19, v21
	global_store_dwordx4 v[24:25], v[18:21], off offset:128
	v_pk_fma_f32 v[24:25], v[62:63], s[24:25], v[14:15] op_sel_hi:[1,0,1]
	v_pk_fma_f32 v[28:29], v[58:59], s[24:25], v[10:11] op_sel_hi:[1,0,1]
	v_cvt_pk_fp8_f32 v18, v24, v25
	v_pk_fma_f32 v[20:21], v[64:65], s[24:25], v[16:17] op_sel_hi:[1,0,1]
	v_pk_fma_f32 v[14:15], v[54:55], s[24:25], v[14:15] op_sel_hi:[1,0,1]
	v_cvt_pk_fp8_f32 v18, v20, v21 op_sel:[0,0,1]
	v_pk_fma_f32 v[10:11], v[50:51], s[24:25], v[10:11] op_sel_hi:[1,0,1]
	v_cvt_pk_fp8_f32 v19, v28, v29
	v_cvt_pk_fp8_f32 v20, v14, v15
	v_cvt_pk_fp8_f32 v21, v10, v11
	v_pk_fma_f32 v[26:27], v[60:61], s[24:25], v[12:13] op_sel_hi:[1,0,1]
	v_pk_fma_f32 v[16:17], v[56:57], s[24:25], v[16:17] op_sel_hi:[1,0,1]
	v_pk_fma_f32 v[12:13], v[52:53], s[24:25], v[12:13] op_sel_hi:[1,0,1]
	v_cvt_pk_fp8_f32 v19, v26, v27 op_sel:[0,0,1]
	v_cvt_pk_fp8_f32 v20, v16, v17 op_sel:[0,0,1]
	v_cvt_pk_fp8_f32 v21, v12, v13 op_sel:[0,0,1]
	s_mov_b64 s[100:101], 0x28000
	v_lshl_add_u64 v[14:15], v[250:251], 0, s[100:101]
	v_pk_fma_f32 v[16:17], v[46:47], s[24:25], v[6:7] op_sel_hi:[1,0,1]
	v_cvt_pk_fp8_f32 v10, v16, v17
	v_permlane16_swap_b32_e32 v18, v20
	v_permlane16_swap_b32_e32 v19, v21
	v_pk_fma_f32 v[12:13], v[48:49], s[24:25], v[8:9] op_sel_hi:[1,0,1]
	global_store_dwordx4 v[14:15], v[18:21], off
	v_cvt_pk_fp8_f32 v10, v12, v13 op_sel:[0,0,1]
	v_pk_fma_f32 v[20:21], v[42:43], s[24:25], v[2:3] op_sel_hi:[1,0,1]
	v_pk_fma_f32 v[6:7], v[38:39], s[24:25], v[6:7] op_sel_hi:[1,0,1]
	v_pk_fma_f32 v[2:3], v[34:35], s[24:25], v[2:3] op_sel_hi:[1,0,1]
	v_cvt_pk_fp8_f32 v11, v20, v21
	v_cvt_pk_fp8_f32 v12, v6, v7
	v_cvt_pk_fp8_f32 v13, v2, v3
	v_pk_fma_f32 v[18:19], v[44:45], s[24:25], v[4:5] op_sel_hi:[1,0,1]
	v_pk_fma_f32 v[8:9], v[40:41], s[24:25], v[8:9] op_sel_hi:[1,0,1]
	v_pk_fma_f32 v[4:5], v[36:37], s[24:25], v[4:5] op_sel_hi:[1,0,1]
	v_cvt_pk_fp8_f32 v11, v18, v19 op_sel:[0,0,1]
	v_cvt_pk_fp8_f32 v12, v8, v9 op_sel:[0,0,1]
	v_cvt_pk_fp8_f32 v13, v4, v5 op_sel:[0,0,1]
	s_mov_b64 s[26:27], -1
	v_permlane16_swap_b32_e32 v10, v12
	v_permlane16_swap_b32_e32 v11, v13
	global_store_dwordx4 v[14:15], v[10:13], off offset:128
	s_cbranch_vccnz .LBB0_39
	s_andn2_b64 vcc, exec, s[38:39]
	s_cbranch_vccnz .LBB0_38
	s_barrier
	s_branch .LBB0_38
